# P0 adaLN k-loop software pipelined (loads of iteration j+3 in flight, x4 unroll, counted vmcnt), stacked on top-k fast path + P11 tile reads
# speedup vs baseline: 1.0095x; 1.0041x over previous
.LBB0_10:
	global_load_dword v8, v[2:3], off offset:-4096
	global_load_dword v9, v[2:3], off offset:-2048
	global_load_dword v10, v[2:3], off
	global_load_dword v11, v[2:3], off offset:2048
	v_add_u32_e32 v12, s16, v4
	v_add_u32_e32 v13, s16, v7
	v_add_u32_e32 v14, s16, v6
	v_add_u32_e32 v15, s16, v5
	s_add_i32 s16, s16, 8
	v_lshl_add_u64 v[2:3], v[2:3], 0, s[14:15]
	s_cmp_eq_u32 s16, 0
	s_waitcnt vmcnt(3)
	v_mul_f32_e32 v16, 0xbfb8aa3b, v8
	s_waitcnt vmcnt(2)
	v_mul_f32_e32 v17, 0xbfb8aa3b, v9
	v_exp_f32_e32 v16, v16
	s_waitcnt vmcnt(1)
	v_mul_f32_e32 v18, 0xbfb8aa3b, v10
	v_exp_f32_e32 v17, v17
	s_waitcnt vmcnt(0)
	v_mul_f32_e32 v19, 0xbfb8aa3b, v11
	v_exp_f32_e32 v18, v18
	v_exp_f32_e32 v19, v19
	v_add_f32_e32 v16, 1.0, v16
	v_add_f32_e32 v17, 1.0, v17
	v_div_scale_f32 v20, s[0:1], v16, v16, v8
	v_add_f32_e32 v18, 1.0, v18
	v_div_scale_f32 v22, s[0:1], v17, v17, v9
	v_rcp_f32_e32 v28, v20
	v_add_f32_e32 v19, 1.0, v19
	v_div_scale_f32 v24, s[2:3], v18, v18, v10
	v_rcp_f32_e32 v29, v22
	v_div_scale_f32 v26, s[4:5], v19, v19, v11
	v_rcp_f32_e32 v30, v24
	v_rcp_f32_e32 v31, v26
	v_fma_f32 v32, -v20, v28, 1.0
	v_div_scale_f32 v21, vcc, v8, v16, v8
	v_fma_f32 v33, -v22, v29, 1.0
	v_fmac_f32_e32 v28, v32, v28
	v_div_scale_f32 v23, s[0:1], v9, v17, v9
	v_fma_f32 v34, -v24, v30, 1.0
	v_fmac_f32_e32 v29, v33, v29
	v_mul_f32_e32 v32, v21, v28
	v_div_scale_f32 v25, s[2:3], v10, v18, v10
	v_fma_f32 v35, -v26, v31, 1.0
	v_fmac_f32_e32 v30, v34, v30
	v_mul_f32_e32 v33, v23, v29
	v_fma_f32 v36, -v20, v32, v21
	v_div_scale_f32 v27, s[4:5], v11, v19, v11
	v_fmac_f32_e32 v31, v35, v31
	v_mul_f32_e32 v34, v25, v30
	v_fma_f32 v37, -v22, v33, v23
	v_fmac_f32_e32 v32, v36, v28
	v_mul_f32_e32 v35, v27, v31
	v_fma_f32 v38, -v24, v34, v25
	v_fmac_f32_e32 v33, v37, v29
	v_fma_f32 v20, -v20, v32, v21
	v_fma_f32 v39, -v26, v35, v27
	v_fmac_f32_e32 v34, v38, v30
	v_fma_f32 v21, -v22, v33, v23
	v_div_fmas_f32 v20, v20, v28, v32
	s_mov_b64 vcc, s[0:1]
	v_fmac_f32_e32 v35, v39, v31
	v_fma_f32 v22, -v24, v34, v25
	v_div_fixup_f32 v8, v20, v16, v8
	v_div_fmas_f32 v16, v21, v29, v33
	s_mov_b64 vcc, s[2:3]
	v_fma_f32 v23, -v26, v35, v27
	ds_write_b32 v12, v8 offset:128
	v_div_fixup_f32 v8, v16, v17, v9
	v_div_fmas_f32 v9, v22, v30, v34
	s_mov_b64 vcc, s[4:5]
	ds_write_b32 v13, v8 offset:128
	v_div_fixup_f32 v8, v9, v18, v10
	v_div_fmas_f32 v9, v23, v31, v35
	ds_write_b32 v14, v8 offset:128
	v_div_fixup_f32 v8, v9, v19, v11
	ds_write_b32 v15, v8 offset:128
	s_cbranch_scc0 .LBB0_10
	s_lshl_b32 s0, s58, 6
	s_add_i32 s1, s0, 0xffffe800
	s_cmpk_lt_u32 s58, 0x60
	v_readlane_b32 s17, v252, 46
	s_cselect_b32 s4, s0, s1
	s_lshl_b32 s14, s17, 7
	s_cmpk_gt_u32 s58, 0x5f
	s_cselect_b64 s[0:1], -1, 0
	s_and_b64 s[2:3], s[0:1], exec
	s_cselect_b32 s2, 0x400, 0
	s_add_i32 s2, s2, s14
	s_mov_b32 s5, 0
	s_mul_hi_u32 s14, s2, 0x6000
	s_mul_i32 s15, s2, 0x6000
	s_lshl_b32 s2, s17, 14
	s_add_i32 s17, s2, 0
	s_lshl_b64 s[2:3], s[4:5], 2
	s_mov_b32 s35, s58
	s_add_u32 s5, s15, s2
	v_readlane_b32 s44, v252, 13
	s_addc_u32 s15, s14, s3
	v_readlane_b32 s50, v252, 19
	v_readlane_b32 s51, v252, 20
	s_add_u32 s14, s50, s5
	v_mov_b32_e32 v3, 0
	v_lshlrev_b32_e32 v2, 2, v174
	s_addc_u32 s15, s51, s15
	s_movk_i32 s16, 0x6000
	v_lshl_add_u64 v[4:5], s[14:15], 0, v[2:3]
	s_mov_b64 s[14:15], 0
	s_mov_b32 s5, 0xc000
	s_mov_b32 s18, 0x12000
	v_mov_b32_e32 v6, v3
	v_mov_b32_e32 v7, v3
	v_mov_b32_e32 v8, v3
	v_mov_b32_e32 v9, v3
	v_mov_b32_e32 v10, v3
	v_mov_b32_e32 v11, v3
	v_mov_b32_e32 v12, v3
	v_mov_b32_e32 v13, v3
	v_mov_b32_e32 v14, v3
	v_mov_b32_e32 v15, v3
	v_mov_b32_e32 v16, v3
	v_mov_b32_e32 v17, v3
	v_mov_b32_e32 v18, v3
	v_mov_b32_e32 v19, v3
	v_mov_b32_e32 v20, v3
	v_mov_b32_e32 v21, v3
	v_mov_b32_e32 v22, v3
	v_mov_b32_e32 v23, v3
	v_mov_b32_e32 v24, v3
	v_mov_b32_e32 v25, v3
	v_mov_b32_e32 v26, v3
	v_mov_b32_e32 v27, v3
	v_mov_b32_e32 v28, v3
	v_mov_b32_e32 v29, v3
	v_mov_b32_e32 v30, v3
	v_mov_b32_e32 v31, v3
	v_mov_b32_e32 v32, v3
	v_mov_b32_e32 v33, v3
	v_mov_b32_e32 v34, v3
	v_mov_b32_e32 v35, v3
	v_mov_b32_e32 v36, v3
	v_mov_b32_e32 v37, v3
	s_waitcnt lgkmcnt(0)
	s_barrier
	v_readlane_b32 s45, v252, 14
	v_readlane_b32 s46, v252, 15
	v_readlane_b32 s47, v252, 16
	v_readlane_b32 s48, v252, 17
	v_readlane_b32 s49, v252, 18
	v_readlane_b32 s52, v252, 21
	v_readlane_b32 s53, v252, 22
	v_readlane_b32 s54, v252, 23
	v_readlane_b32 s55, v252, 24
	v_readlane_b32 s56, v252, 25
	v_readlane_b32 s57, v252, 26
	v_readlane_b32 s58, v252, 27
	v_readlane_b32 s59, v252, 28
	s_mov_b32 s25, 0
	s_mov_b32 s24, 0x0
	v_lshl_add_u64 v[210:211], v[4:5], 0, s[24:25]
	v_add_co_u32_e32 v212, vcc, s16, v210
	global_load_dword v178, v[210:211], off
	s_nop 0
	v_addc_co_u32_e32 v213, vcc, 0, v211, vcc
	v_add_co_u32_e32 v214, vcc, s5, v210
	s_nop 1
	v_addc_co_u32_e32 v215, vcc, 0, v211, vcc
	v_add_co_u32_e32 v216, vcc, s18, v210
	s_nop 1
	v_addc_co_u32_e32 v217, vcc, 0, v211, vcc
	global_load_dword v180, v[212:213], off
	global_load_dword v182, v[214:215], off
	global_load_dword v184, v[216:217], off
	s_mov_b32 s24, 0x18000
	v_lshl_add_u64 v[210:211], v[4:5], 0, s[24:25]
	v_add_co_u32_e32 v212, vcc, s16, v210
	global_load_dword v186, v[210:211], off
	s_nop 0
	v_addc_co_u32_e32 v213, vcc, 0, v211, vcc
	v_add_co_u32_e32 v214, vcc, s5, v210
	s_nop 1
	v_addc_co_u32_e32 v215, vcc, 0, v211, vcc
	v_add_co_u32_e32 v216, vcc, s18, v210
	s_nop 1
	v_addc_co_u32_e32 v217, vcc, 0, v211, vcc
	global_load_dword v188, v[212:213], off
	global_load_dword v190, v[214:215], off
	global_load_dword v192, v[216:217], off
	s_mov_b32 s24, 0x30000
	v_lshl_add_u64 v[210:211], v[4:5], 0, s[24:25]
	v_add_co_u32_e32 v212, vcc, s16, v210
	global_load_dword v194, v[210:211], off
	s_nop 0
	v_addc_co_u32_e32 v213, vcc, 0, v211, vcc
	v_add_co_u32_e32 v214, vcc, s5, v210
	s_nop 1
	v_addc_co_u32_e32 v215, vcc, 0, v211, vcc
	v_add_co_u32_e32 v216, vcc, s18, v210
	s_nop 1
	v_addc_co_u32_e32 v217, vcc, 0, v211, vcc
	global_load_dword v196, v[212:213], off
	global_load_dword v198, v[214:215], off
	global_load_dword v200, v[216:217], off
.LBB0_12:
	s_add_u32 s24, s14, 0x48000
	s_min_u32 s24, s24, 0x2e8000
	v_lshl_add_u64 v[210:211], v[4:5], 0, s[24:25]
	v_add_co_u32_e32 v212, vcc, s16, v210
	global_load_dword v202, v[210:211], off
	s_nop 0
	v_addc_co_u32_e32 v213, vcc, 0, v211, vcc
	v_add_co_u32_e32 v214, vcc, s5, v210
	s_nop 1
	v_addc_co_u32_e32 v215, vcc, 0, v211, vcc
	v_add_co_u32_e32 v216, vcc, s18, v210
	s_nop 1
	v_addc_co_u32_e32 v217, vcc, 0, v211, vcc
	global_load_dword v204, v[212:213], off
	global_load_dword v206, v[214:215], off
	global_load_dword v208, v[216:217], off
	v_mov_b32_e32 v3, s17
	ds_read_b128 v[42:45], v3
	ds_read_b128 v[46:49], v3 offset:16
	ds_read_b128 v[50:53], v3 offset:32
	ds_read_b128 v[54:57], v3 offset:48
	ds_read_b128 v[58:61], v3 offset:64
	ds_read_b128 v[62:65], v3 offset:80
	ds_read_b128 v[66:69], v3 offset:96
	ds_read_b128 v[70:73], v3 offset:112
	ds_read_b128 v[74:77], v3 offset:128
	ds_read_b128 v[78:81], v3 offset:144
	ds_read_b128 v[82:85], v3 offset:160
	ds_read_b128 v[86:89], v3 offset:176
	ds_read_b128 v[90:93], v3 offset:192
	ds_read_b128 v[94:97], v3 offset:208
	ds_read_b128 v[98:101], v3 offset:224
	ds_read_b128 v[102:105], v3 offset:240
	ds_read_b128 v[106:109], v3 offset:256
	ds_read_b128 v[110:113], v3 offset:272
	ds_read_b128 v[114:117], v3 offset:288
	ds_read_b128 v[118:121], v3 offset:304
	ds_read_b128 v[122:125], v3 offset:320
	ds_read_b128 v[126:129], v3 offset:336
	ds_read_b128 v[130:133], v3 offset:352
	ds_read_b128 v[134:137], v3 offset:368
	ds_read_b128 v[138:141], v3 offset:384
	ds_read_b128 v[142:145], v3 offset:400
	ds_read_b128 v[146:149], v3 offset:416
	ds_read_b128 v[150:153], v3 offset:432
	ds_read_b128 v[154:157], v3 offset:448
	ds_read_b128 v[158:161], v3 offset:464
	ds_read_b128 v[162:165], v3 offset:480
	ds_read_b128 v[166:169], v3 offset:496
	s_addk_i32 s17, 0x200
	s_add_u32 s14, s14, 0x18000
	s_addc_u32 s15, s15, 0
	s_cmp_eq_u32 s14, 0x300000
	s_waitcnt vmcnt(15) lgkmcnt(14)
	v_pk_fma_f32 v[8:9], v[178:179], v[42:43], v[8:9] op_sel_hi:[0,1,1]
	v_pk_fma_f32 v[10:11], v[178:179], v[44:45], v[10:11] op_sel_hi:[0,1,1]
	v_pk_fma_f32 v[12:13], v[178:179], v[46:47], v[12:13] op_sel_hi:[0,1,1]
	v_pk_fma_f32 v[14:15], v[178:179], v[48:49], v[14:15] op_sel_hi:[0,1,1]
	v_pk_fma_f32 v[16:17], v[178:179], v[50:51], v[16:17] op_sel_hi:[0,1,1]
	v_pk_fma_f32 v[18:19], v[178:179], v[52:53], v[18:19] op_sel_hi:[0,1,1]
	v_pk_fma_f32 v[20:21], v[178:179], v[54:55], v[20:21] op_sel_hi:[0,1,1]
	v_pk_fma_f32 v[22:23], v[178:179], v[56:57], v[22:23] op_sel_hi:[0,1,1]
	v_pk_fma_f32 v[24:25], v[178:179], v[58:59], v[24:25] op_sel_hi:[0,1,1]
	v_pk_fma_f32 v[26:27], v[178:179], v[60:61], v[26:27] op_sel_hi:[0,1,1]
	v_pk_fma_f32 v[28:29], v[178:179], v[62:63], v[28:29] op_sel_hi:[0,1,1]
	v_pk_fma_f32 v[30:31], v[178:179], v[64:65], v[30:31] op_sel_hi:[0,1,1]
	v_pk_fma_f32 v[32:33], v[178:179], v[66:67], v[32:33] op_sel_hi:[0,1,1]
	v_pk_fma_f32 v[34:35], v[178:179], v[68:69], v[34:35] op_sel_hi:[0,1,1]
	v_pk_fma_f32 v[36:37], v[178:179], v[70:71], v[36:37] op_sel_hi:[0,1,1]
	v_pk_fma_f32 v[6:7], v[178:179], v[72:73], v[6:7] op_sel_hi:[0,1,1]
	s_waitcnt vmcnt(14)
	v_pk_fma_f32 v[8:9], v[180:181], v[74:75], v[8:9] op_sel_hi:[0,1,1]
	v_pk_fma_f32 v[10:11], v[180:181], v[76:77], v[10:11] op_sel_hi:[0,1,1]
	v_pk_fma_f32 v[12:13], v[180:181], v[78:79], v[12:13] op_sel_hi:[0,1,1]
	v_pk_fma_f32 v[14:15], v[180:181], v[80:81], v[14:15] op_sel_hi:[0,1,1]
	v_pk_fma_f32 v[16:17], v[180:181], v[82:83], v[16:17] op_sel_hi:[0,1,1]
	v_pk_fma_f32 v[18:19], v[180:181], v[84:85], v[18:19] op_sel_hi:[0,1,1]
	v_pk_fma_f32 v[20:21], v[180:181], v[86:87], v[20:21] op_sel_hi:[0,1,1]
	v_pk_fma_f32 v[22:23], v[180:181], v[88:89], v[22:23] op_sel_hi:[0,1,1]
	v_pk_fma_f32 v[24:25], v[180:181], v[90:91], v[24:25] op_sel_hi:[0,1,1]
	v_pk_fma_f32 v[26:27], v[180:181], v[92:93], v[26:27] op_sel_hi:[0,1,1]
	v_pk_fma_f32 v[28:29], v[180:181], v[94:95], v[28:29] op_sel_hi:[0,1,1]
	v_pk_fma_f32 v[30:31], v[180:181], v[96:97], v[30:31] op_sel_hi:[0,1,1]
	v_pk_fma_f32 v[32:33], v[180:181], v[98:99], v[32:33] op_sel_hi:[0,1,1]
	v_pk_fma_f32 v[34:35], v[180:181], v[100:101], v[34:35] op_sel_hi:[0,1,1]
	v_pk_fma_f32 v[36:37], v[180:181], v[102:103], v[36:37] op_sel_hi:[0,1,1]
	v_pk_fma_f32 v[6:7], v[180:181], v[104:105], v[6:7] op_sel_hi:[0,1,1]
	s_waitcnt vmcnt(13)
	v_pk_fma_f32 v[8:9], v[182:183], v[106:107], v[8:9] op_sel_hi:[0,1,1]
	v_pk_fma_f32 v[10:11], v[182:183], v[108:109], v[10:11] op_sel_hi:[0,1,1]
	v_pk_fma_f32 v[12:13], v[182:183], v[110:111], v[12:13] op_sel_hi:[0,1,1]
	v_pk_fma_f32 v[14:15], v[182:183], v[112:113], v[14:15] op_sel_hi:[0,1,1]
	s_waitcnt lgkmcnt(13)
	v_pk_fma_f32 v[16:17], v[182:183], v[114:115], v[16:17] op_sel_hi:[0,1,1]
	v_pk_fma_f32 v[18:19], v[182:183], v[116:117], v[18:19] op_sel_hi:[0,1,1]
	s_waitcnt lgkmcnt(12)
	v_pk_fma_f32 v[20:21], v[182:183], v[118:119], v[20:21] op_sel_hi:[0,1,1]
	v_pk_fma_f32 v[22:23], v[182:183], v[120:121], v[22:23] op_sel_hi:[0,1,1]
	s_waitcnt lgkmcnt(11)
	v_pk_fma_f32 v[24:25], v[182:183], v[122:123], v[24:25] op_sel_hi:[0,1,1]
	v_pk_fma_f32 v[26:27], v[182:183], v[124:125], v[26:27] op_sel_hi:[0,1,1]
	s_waitcnt lgkmcnt(10)
	v_pk_fma_f32 v[28:29], v[182:183], v[126:127], v[28:29] op_sel_hi:[0,1,1]
	v_pk_fma_f32 v[30:31], v[182:183], v[128:129], v[30:31] op_sel_hi:[0,1,1]
	s_waitcnt lgkmcnt(9)
	v_pk_fma_f32 v[32:33], v[182:183], v[130:131], v[32:33] op_sel_hi:[0,1,1]
	v_pk_fma_f32 v[34:35], v[182:183], v[132:133], v[34:35] op_sel_hi:[0,1,1]
	s_waitcnt lgkmcnt(8)
	v_pk_fma_f32 v[36:37], v[182:183], v[134:135], v[36:37] op_sel_hi:[0,1,1]
	v_pk_fma_f32 v[6:7], v[182:183], v[136:137], v[6:7] op_sel_hi:[0,1,1]
	s_waitcnt vmcnt(12) lgkmcnt(7)
	v_pk_fma_f32 v[8:9], v[184:185], v[138:139], v[8:9] op_sel_hi:[0,1,1]
	v_pk_fma_f32 v[10:11], v[184:185], v[140:141], v[10:11] op_sel_hi:[0,1,1]
	s_waitcnt lgkmcnt(6)
	v_pk_fma_f32 v[12:13], v[184:185], v[142:143], v[12:13] op_sel_hi:[0,1,1]
	v_pk_fma_f32 v[14:15], v[184:185], v[144:145], v[14:15] op_sel_hi:[0,1,1]
	s_waitcnt lgkmcnt(5)
	v_pk_fma_f32 v[16:17], v[184:185], v[146:147], v[16:17] op_sel_hi:[0,1,1]
	v_pk_fma_f32 v[18:19], v[184:185], v[148:149], v[18:19] op_sel_hi:[0,1,1]
	s_waitcnt lgkmcnt(4)
	v_pk_fma_f32 v[20:21], v[184:185], v[150:151], v[20:21] op_sel_hi:[0,1,1]
	v_pk_fma_f32 v[22:23], v[184:185], v[152:153], v[22:23] op_sel_hi:[0,1,1]
	s_waitcnt lgkmcnt(3)
	v_pk_fma_f32 v[24:25], v[184:185], v[154:155], v[24:25] op_sel_hi:[0,1,1]
	v_pk_fma_f32 v[26:27], v[184:185], v[156:157], v[26:27] op_sel_hi:[0,1,1]
	s_waitcnt lgkmcnt(2)
	v_pk_fma_f32 v[28:29], v[184:185], v[158:159], v[28:29] op_sel_hi:[0,1,1]
	v_pk_fma_f32 v[30:31], v[184:185], v[160:161], v[30:31] op_sel_hi:[0,1,1]
	s_waitcnt lgkmcnt(1)
	v_pk_fma_f32 v[32:33], v[184:185], v[162:163], v[32:33] op_sel_hi:[0,1,1]
	v_pk_fma_f32 v[34:35], v[184:185], v[164:165], v[34:35] op_sel_hi:[0,1,1]
	s_waitcnt lgkmcnt(0)
	v_pk_fma_f32 v[36:37], v[184:185], v[166:167], v[36:37] op_sel_hi:[0,1,1]
	v_pk_fma_f32 v[6:7], v[184:185], v[168:169], v[6:7] op_sel_hi:[0,1,1]
	s_add_u32 s24, s14, 0x48000
	s_min_u32 s24, s24, 0x2e8000
	v_lshl_add_u64 v[210:211], v[4:5], 0, s[24:25]
	v_add_co_u32_e32 v212, vcc, s16, v210
	global_load_dword v178, v[210:211], off
	s_nop 0
	v_addc_co_u32_e32 v213, vcc, 0, v211, vcc
	v_add_co_u32_e32 v214, vcc, s5, v210
	s_nop 1
	v_addc_co_u32_e32 v215, vcc, 0, v211, vcc
	v_add_co_u32_e32 v216, vcc, s18, v210
	s_nop 1
	v_addc_co_u32_e32 v217, vcc, 0, v211, vcc
	global_load_dword v180, v[212:213], off
	global_load_dword v182, v[214:215], off
	global_load_dword v184, v[216:217], off
	v_mov_b32_e32 v3, s17
	ds_read_b128 v[42:45], v3
	ds_read_b128 v[46:49], v3 offset:16
	ds_read_b128 v[50:53], v3 offset:32
	ds_read_b128 v[54:57], v3 offset:48
	ds_read_b128 v[58:61], v3 offset:64
	ds_read_b128 v[62:65], v3 offset:80
	ds_read_b128 v[66:69], v3 offset:96
	ds_read_b128 v[70:73], v3 offset:112
	ds_read_b128 v[74:77], v3 offset:128
	ds_read_b128 v[78:81], v3 offset:144
	ds_read_b128 v[82:85], v3 offset:160
	ds_read_b128 v[86:89], v3 offset:176
	ds_read_b128 v[90:93], v3 offset:192
	ds_read_b128 v[94:97], v3 offset:208
	ds_read_b128 v[98:101], v3 offset:224
	ds_read_b128 v[102:105], v3 offset:240
	ds_read_b128 v[106:109], v3 offset:256
	ds_read_b128 v[110:113], v3 offset:272
	ds_read_b128 v[114:117], v3 offset:288
	ds_read_b128 v[118:121], v3 offset:304
	ds_read_b128 v[122:125], v3 offset:320
	ds_read_b128 v[126:129], v3 offset:336
	ds_read_b128 v[130:133], v3 offset:352
	ds_read_b128 v[134:137], v3 offset:368
	ds_read_b128 v[138:141], v3 offset:384
	ds_read_b128 v[142:145], v3 offset:400
	ds_read_b128 v[146:149], v3 offset:416
	ds_read_b128 v[150:153], v3 offset:432
	ds_read_b128 v[154:157], v3 offset:448
	ds_read_b128 v[158:161], v3 offset:464
	ds_read_b128 v[162:165], v3 offset:480
	ds_read_b128 v[166:169], v3 offset:496
	s_addk_i32 s17, 0x200
	s_add_u32 s14, s14, 0x18000
	s_addc_u32 s15, s15, 0
	s_cmp_eq_u32 s14, 0x300000
	s_waitcnt vmcnt(15) lgkmcnt(14)
	v_pk_fma_f32 v[8:9], v[186:187], v[42:43], v[8:9] op_sel_hi:[0,1,1]
	v_pk_fma_f32 v[10:11], v[186:187], v[44:45], v[10:11] op_sel_hi:[0,1,1]
	v_pk_fma_f32 v[12:13], v[186:187], v[46:47], v[12:13] op_sel_hi:[0,1,1]
	v_pk_fma_f32 v[14:15], v[186:187], v[48:49], v[14:15] op_sel_hi:[0,1,1]
	v_pk_fma_f32 v[16:17], v[186:187], v[50:51], v[16:17] op_sel_hi:[0,1,1]
	v_pk_fma_f32 v[18:19], v[186:187], v[52:53], v[18:19] op_sel_hi:[0,1,1]
	v_pk_fma_f32 v[20:21], v[186:187], v[54:55], v[20:21] op_sel_hi:[0,1,1]
	v_pk_fma_f32 v[22:23], v[186:187], v[56:57], v[22:23] op_sel_hi:[0,1,1]
	v_pk_fma_f32 v[24:25], v[186:187], v[58:59], v[24:25] op_sel_hi:[0,1,1]
	v_pk_fma_f32 v[26:27], v[186:187], v[60:61], v[26:27] op_sel_hi:[0,1,1]
	v_pk_fma_f32 v[28:29], v[186:187], v[62:63], v[28:29] op_sel_hi:[0,1,1]
	v_pk_fma_f32 v[30:31], v[186:187], v[64:65], v[30:31] op_sel_hi:[0,1,1]
	v_pk_fma_f32 v[32:33], v[186:187], v[66:67], v[32:33] op_sel_hi:[0,1,1]
	v_pk_fma_f32 v[34:35], v[186:187], v[68:69], v[34:35] op_sel_hi:[0,1,1]
	v_pk_fma_f32 v[36:37], v[186:187], v[70:71], v[36:37] op_sel_hi:[0,1,1]
	v_pk_fma_f32 v[6:7], v[186:187], v[72:73], v[6:7] op_sel_hi:[0,1,1]
	s_waitcnt vmcnt(14)
	v_pk_fma_f32 v[8:9], v[188:189], v[74:75], v[8:9] op_sel_hi:[0,1,1]
	v_pk_fma_f32 v[10:11], v[188:189], v[76:77], v[10:11] op_sel_hi:[0,1,1]
	v_pk_fma_f32 v[12:13], v[188:189], v[78:79], v[12:13] op_sel_hi:[0,1,1]
	v_pk_fma_f32 v[14:15], v[188:189], v[80:81], v[14:15] op_sel_hi:[0,1,1]
	v_pk_fma_f32 v[16:17], v[188:189], v[82:83], v[16:17] op_sel_hi:[0,1,1]
	v_pk_fma_f32 v[18:19], v[188:189], v[84:85], v[18:19] op_sel_hi:[0,1,1]
	v_pk_fma_f32 v[20:21], v[188:189], v[86:87], v[20:21] op_sel_hi:[0,1,1]
	v_pk_fma_f32 v[22:23], v[188:189], v[88:89], v[22:23] op_sel_hi:[0,1,1]
	v_pk_fma_f32 v[24:25], v[188:189], v[90:91], v[24:25] op_sel_hi:[0,1,1]
	v_pk_fma_f32 v[26:27], v[188:189], v[92:93], v[26:27] op_sel_hi:[0,1,1]
	v_pk_fma_f32 v[28:29], v[188:189], v[94:95], v[28:29] op_sel_hi:[0,1,1]
	v_pk_fma_f32 v[30:31], v[188:189], v[96:97], v[30:31] op_sel_hi:[0,1,1]
	v_pk_fma_f32 v[32:33], v[188:189], v[98:99], v[32:33] op_sel_hi:[0,1,1]
	v_pk_fma_f32 v[34:35], v[188:189], v[100:101], v[34:35] op_sel_hi:[0,1,1]
	v_pk_fma_f32 v[36:37], v[188:189], v[102:103], v[36:37] op_sel_hi:[0,1,1]
	v_pk_fma_f32 v[6:7], v[188:189], v[104:105], v[6:7] op_sel_hi:[0,1,1]
	s_waitcnt vmcnt(13)
	v_pk_fma_f32 v[8:9], v[190:191], v[106:107], v[8:9] op_sel_hi:[0,1,1]
	v_pk_fma_f32 v[10:11], v[190:191], v[108:109], v[10:11] op_sel_hi:[0,1,1]
	v_pk_fma_f32 v[12:13], v[190:191], v[110:111], v[12:13] op_sel_hi:[0,1,1]
	v_pk_fma_f32 v[14:15], v[190:191], v[112:113], v[14:15] op_sel_hi:[0,1,1]
	s_waitcnt lgkmcnt(13)
	v_pk_fma_f32 v[16:17], v[190:191], v[114:115], v[16:17] op_sel_hi:[0,1,1]
	v_pk_fma_f32 v[18:19], v[190:191], v[116:117], v[18:19] op_sel_hi:[0,1,1]
	s_waitcnt lgkmcnt(12)
	v_pk_fma_f32 v[20:21], v[190:191], v[118:119], v[20:21] op_sel_hi:[0,1,1]
	v_pk_fma_f32 v[22:23], v[190:191], v[120:121], v[22:23] op_sel_hi:[0,1,1]
	s_waitcnt lgkmcnt(11)
	v_pk_fma_f32 v[24:25], v[190:191], v[122:123], v[24:25] op_sel_hi:[0,1,1]
	v_pk_fma_f32 v[26:27], v[190:191], v[124:125], v[26:27] op_sel_hi:[0,1,1]
	s_waitcnt lgkmcnt(10)
	v_pk_fma_f32 v[28:29], v[190:191], v[126:127], v[28:29] op_sel_hi:[0,1,1]
	v_pk_fma_f32 v[30:31], v[190:191], v[128:129], v[30:31] op_sel_hi:[0,1,1]
	s_waitcnt lgkmcnt(9)
	v_pk_fma_f32 v[32:33], v[190:191], v[130:131], v[32:33] op_sel_hi:[0,1,1]
	v_pk_fma_f32 v[34:35], v[190:191], v[132:133], v[34:35] op_sel_hi:[0,1,1]
	s_waitcnt lgkmcnt(8)
	v_pk_fma_f32 v[36:37], v[190:191], v[134:135], v[36:37] op_sel_hi:[0,1,1]
	v_pk_fma_f32 v[6:7], v[190:191], v[136:137], v[6:7] op_sel_hi:[0,1,1]
	s_waitcnt vmcnt(12) lgkmcnt(7)
	v_pk_fma_f32 v[8:9], v[192:193], v[138:139], v[8:9] op_sel_hi:[0,1,1]
	v_pk_fma_f32 v[10:11], v[192:193], v[140:141], v[10:11] op_sel_hi:[0,1,1]
	s_waitcnt lgkmcnt(6)
	v_pk_fma_f32 v[12:13], v[192:193], v[142:143], v[12:13] op_sel_hi:[0,1,1]
	v_pk_fma_f32 v[14:15], v[192:193], v[144:145], v[14:15] op_sel_hi:[0,1,1]
	s_waitcnt lgkmcnt(5)
	v_pk_fma_f32 v[16:17], v[192:193], v[146:147], v[16:17] op_sel_hi:[0,1,1]
	v_pk_fma_f32 v[18:19], v[192:193], v[148:149], v[18:19] op_sel_hi:[0,1,1]
	s_waitcnt lgkmcnt(4)
	v_pk_fma_f32 v[20:21], v[192:193], v[150:151], v[20:21] op_sel_hi:[0,1,1]
	v_pk_fma_f32 v[22:23], v[192:193], v[152:153], v[22:23] op_sel_hi:[0,1,1]
	s_waitcnt lgkmcnt(3)
	v_pk_fma_f32 v[24:25], v[192:193], v[154:155], v[24:25] op_sel_hi:[0,1,1]
	v_pk_fma_f32 v[26:27], v[192:193], v[156:157], v[26:27] op_sel_hi:[0,1,1]
	s_waitcnt lgkmcnt(2)
	v_pk_fma_f32 v[28:29], v[192:193], v[158:159], v[28:29] op_sel_hi:[0,1,1]
	v_pk_fma_f32 v[30:31], v[192:193], v[160:161], v[30:31] op_sel_hi:[0,1,1]
	s_waitcnt lgkmcnt(1)
	v_pk_fma_f32 v[32:33], v[192:193], v[162:163], v[32:33] op_sel_hi:[0,1,1]
	v_pk_fma_f32 v[34:35], v[192:193], v[164:165], v[34:35] op_sel_hi:[0,1,1]
	s_waitcnt lgkmcnt(0)
	v_pk_fma_f32 v[36:37], v[192:193], v[166:167], v[36:37] op_sel_hi:[0,1,1]
	v_pk_fma_f32 v[6:7], v[192:193], v[168:169], v[6:7] op_sel_hi:[0,1,1]
	s_add_u32 s24, s14, 0x48000
	s_min_u32 s24, s24, 0x2e8000
	v_lshl_add_u64 v[210:211], v[4:5], 0, s[24:25]
	v_add_co_u32_e32 v212, vcc, s16, v210
	global_load_dword v186, v[210:211], off
	s_nop 0
	v_addc_co_u32_e32 v213, vcc, 0, v211, vcc
	v_add_co_u32_e32 v214, vcc, s5, v210
	s_nop 1
	v_addc_co_u32_e32 v215, vcc, 0, v211, vcc
	v_add_co_u32_e32 v216, vcc, s18, v210
	s_nop 1
	v_addc_co_u32_e32 v217, vcc, 0, v211, vcc
	global_load_dword v188, v[212:213], off
	global_load_dword v190, v[214:215], off
	global_load_dword v192, v[216:217], off
	v_mov_b32_e32 v3, s17
	ds_read_b128 v[42:45], v3
	ds_read_b128 v[46:49], v3 offset:16
	ds_read_b128 v[50:53], v3 offset:32
	ds_read_b128 v[54:57], v3 offset:48
	ds_read_b128 v[58:61], v3 offset:64
	ds_read_b128 v[62:65], v3 offset:80
	ds_read_b128 v[66:69], v3 offset:96
	ds_read_b128 v[70:73], v3 offset:112
	ds_read_b128 v[74:77], v3 offset:128
	ds_read_b128 v[78:81], v3 offset:144
	ds_read_b128 v[82:85], v3 offset:160
	ds_read_b128 v[86:89], v3 offset:176
	ds_read_b128 v[90:93], v3 offset:192
	ds_read_b128 v[94:97], v3 offset:208
	ds_read_b128 v[98:101], v3 offset:224
	ds_read_b128 v[102:105], v3 offset:240
	ds_read_b128 v[106:109], v3 offset:256
	ds_read_b128 v[110:113], v3 offset:272
	ds_read_b128 v[114:117], v3 offset:288
	ds_read_b128 v[118:121], v3 offset:304
	ds_read_b128 v[122:125], v3 offset:320
	ds_read_b128 v[126:129], v3 offset:336
	ds_read_b128 v[130:133], v3 offset:352
	ds_read_b128 v[134:137], v3 offset:368
	ds_read_b128 v[138:141], v3 offset:384
	ds_read_b128 v[142:145], v3 offset:400
	ds_read_b128 v[146:149], v3 offset:416
	ds_read_b128 v[150:153], v3 offset:432
	ds_read_b128 v[154:157], v3 offset:448
	ds_read_b128 v[158:161], v3 offset:464
	ds_read_b128 v[162:165], v3 offset:480
	ds_read_b128 v[166:169], v3 offset:496
	s_addk_i32 s17, 0x200
	s_add_u32 s14, s14, 0x18000
	s_addc_u32 s15, s15, 0
	s_cmp_eq_u32 s14, 0x300000
	s_waitcnt vmcnt(15) lgkmcnt(14)
	v_pk_fma_f32 v[8:9], v[194:195], v[42:43], v[8:9] op_sel_hi:[0,1,1]
	v_pk_fma_f32 v[10:11], v[194:195], v[44:45], v[10:11] op_sel_hi:[0,1,1]
	v_pk_fma_f32 v[12:13], v[194:195], v[46:47], v[12:13] op_sel_hi:[0,1,1]
	v_pk_fma_f32 v[14:15], v[194:195], v[48:49], v[14:15] op_sel_hi:[0,1,1]
	v_pk_fma_f32 v[16:17], v[194:195], v[50:51], v[16:17] op_sel_hi:[0,1,1]
	v_pk_fma_f32 v[18:19], v[194:195], v[52:53], v[18:19] op_sel_hi:[0,1,1]
	v_pk_fma_f32 v[20:21], v[194:195], v[54:55], v[20:21] op_sel_hi:[0,1,1]
	v_pk_fma_f32 v[22:23], v[194:195], v[56:57], v[22:23] op_sel_hi:[0,1,1]
	v_pk_fma_f32 v[24:25], v[194:195], v[58:59], v[24:25] op_sel_hi:[0,1,1]
	v_pk_fma_f32 v[26:27], v[194:195], v[60:61], v[26:27] op_sel_hi:[0,1,1]
	v_pk_fma_f32 v[28:29], v[194:195], v[62:63], v[28:29] op_sel_hi:[0,1,1]
	v_pk_fma_f32 v[30:31], v[194:195], v[64:65], v[30:31] op_sel_hi:[0,1,1]
	v_pk_fma_f32 v[32:33], v[194:195], v[66:67], v[32:33] op_sel_hi:[0,1,1]
	v_pk_fma_f32 v[34:35], v[194:195], v[68:69], v[34:35] op_sel_hi:[0,1,1]
	v_pk_fma_f32 v[36:37], v[194:195], v[70:71], v[36:37] op_sel_hi:[0,1,1]
	v_pk_fma_f32 v[6:7], v[194:195], v[72:73], v[6:7] op_sel_hi:[0,1,1]
	s_waitcnt vmcnt(14)
	v_pk_fma_f32 v[8:9], v[196:197], v[74:75], v[8:9] op_sel_hi:[0,1,1]
	v_pk_fma_f32 v[10:11], v[196:197], v[76:77], v[10:11] op_sel_hi:[0,1,1]
	v_pk_fma_f32 v[12:13], v[196:197], v[78:79], v[12:13] op_sel_hi:[0,1,1]
	v_pk_fma_f32 v[14:15], v[196:197], v[80:81], v[14:15] op_sel_hi:[0,1,1]
	v_pk_fma_f32 v[16:17], v[196:197], v[82:83], v[16:17] op_sel_hi:[0,1,1]
	v_pk_fma_f32 v[18:19], v[196:197], v[84:85], v[18:19] op_sel_hi:[0,1,1]
	v_pk_fma_f32 v[20:21], v[196:197], v[86:87], v[20:21] op_sel_hi:[0,1,1]
	v_pk_fma_f32 v[22:23], v[196:197], v[88:89], v[22:23] op_sel_hi:[0,1,1]
	v_pk_fma_f32 v[24:25], v[196:197], v[90:91], v[24:25] op_sel_hi:[0,1,1]
	v_pk_fma_f32 v[26:27], v[196:197], v[92:93], v[26:27] op_sel_hi:[0,1,1]
	v_pk_fma_f32 v[28:29], v[196:197], v[94:95], v[28:29] op_sel_hi:[0,1,1]
	v_pk_fma_f32 v[30:31], v[196:197], v[96:97], v[30:31] op_sel_hi:[0,1,1]
	v_pk_fma_f32 v[32:33], v[196:197], v[98:99], v[32:33] op_sel_hi:[0,1,1]
	v_pk_fma_f32 v[34:35], v[196:197], v[100:101], v[34:35] op_sel_hi:[0,1,1]
	v_pk_fma_f32 v[36:37], v[196:197], v[102:103], v[36:37] op_sel_hi:[0,1,1]
	v_pk_fma_f32 v[6:7], v[196:197], v[104:105], v[6:7] op_sel_hi:[0,1,1]
	s_waitcnt vmcnt(13)
	v_pk_fma_f32 v[8:9], v[198:199], v[106:107], v[8:9] op_sel_hi:[0,1,1]
	v_pk_fma_f32 v[10:11], v[198:199], v[108:109], v[10:11] op_sel_hi:[0,1,1]
	v_pk_fma_f32 v[12:13], v[198:199], v[110:111], v[12:13] op_sel_hi:[0,1,1]
	v_pk_fma_f32 v[14:15], v[198:199], v[112:113], v[14:15] op_sel_hi:[0,1,1]
	s_waitcnt lgkmcnt(13)
	v_pk_fma_f32 v[16:17], v[198:199], v[114:115], v[16:17] op_sel_hi:[0,1,1]
	v_pk_fma_f32 v[18:19], v[198:199], v[116:117], v[18:19] op_sel_hi:[0,1,1]
	s_waitcnt lgkmcnt(12)
	v_pk_fma_f32 v[20:21], v[198:199], v[118:119], v[20:21] op_sel_hi:[0,1,1]
	v_pk_fma_f32 v[22:23], v[198:199], v[120:121], v[22:23] op_sel_hi:[0,1,1]
	s_waitcnt lgkmcnt(11)
	v_pk_fma_f32 v[24:25], v[198:199], v[122:123], v[24:25] op_sel_hi:[0,1,1]
	v_pk_fma_f32 v[26:27], v[198:199], v[124:125], v[26:27] op_sel_hi:[0,1,1]
	s_waitcnt lgkmcnt(10)
	v_pk_fma_f32 v[28:29], v[198:199], v[126:127], v[28:29] op_sel_hi:[0,1,1]
	v_pk_fma_f32 v[30:31], v[198:199], v[128:129], v[30:31] op_sel_hi:[0,1,1]
	s_waitcnt lgkmcnt(9)
	v_pk_fma_f32 v[32:33], v[198:199], v[130:131], v[32:33] op_sel_hi:[0,1,1]
	v_pk_fma_f32 v[34:35], v[198:199], v[132:133], v[34:35] op_sel_hi:[0,1,1]
	s_waitcnt lgkmcnt(8)
	v_pk_fma_f32 v[36:37], v[198:199], v[134:135], v[36:37] op_sel_hi:[0,1,1]
	v_pk_fma_f32 v[6:7], v[198:199], v[136:137], v[6:7] op_sel_hi:[0,1,1]
	s_waitcnt vmcnt(12) lgkmcnt(7)
	v_pk_fma_f32 v[8:9], v[200:201], v[138:139], v[8:9] op_sel_hi:[0,1,1]
	v_pk_fma_f32 v[10:11], v[200:201], v[140:141], v[10:11] op_sel_hi:[0,1,1]
	s_waitcnt lgkmcnt(6)
	v_pk_fma_f32 v[12:13], v[200:201], v[142:143], v[12:13] op_sel_hi:[0,1,1]
	v_pk_fma_f32 v[14:15], v[200:201], v[144:145], v[14:15] op_sel_hi:[0,1,1]
	s_waitcnt lgkmcnt(5)
	v_pk_fma_f32 v[16:17], v[200:201], v[146:147], v[16:17] op_sel_hi:[0,1,1]
	v_pk_fma_f32 v[18:19], v[200:201], v[148:149], v[18:19] op_sel_hi:[0,1,1]
	s_waitcnt lgkmcnt(4)
	v_pk_fma_f32 v[20:21], v[200:201], v[150:151], v[20:21] op_sel_hi:[0,1,1]
	v_pk_fma_f32 v[22:23], v[200:201], v[152:153], v[22:23] op_sel_hi:[0,1,1]
	s_waitcnt lgkmcnt(3)
	v_pk_fma_f32 v[24:25], v[200:201], v[154:155], v[24:25] op_sel_hi:[0,1,1]
	v_pk_fma_f32 v[26:27], v[200:201], v[156:157], v[26:27] op_sel_hi:[0,1,1]
	s_waitcnt lgkmcnt(2)
	v_pk_fma_f32 v[28:29], v[200:201], v[158:159], v[28:29] op_sel_hi:[0,1,1]
	v_pk_fma_f32 v[30:31], v[200:201], v[160:161], v[30:31] op_sel_hi:[0,1,1]
	s_waitcnt lgkmcnt(1)
	v_pk_fma_f32 v[32:33], v[200:201], v[162:163], v[32:33] op_sel_hi:[0,1,1]
	v_pk_fma_f32 v[34:35], v[200:201], v[164:165], v[34:35] op_sel_hi:[0,1,1]
	s_waitcnt lgkmcnt(0)
	v_pk_fma_f32 v[36:37], v[200:201], v[166:167], v[36:37] op_sel_hi:[0,1,1]
	v_pk_fma_f32 v[6:7], v[200:201], v[168:169], v[6:7] op_sel_hi:[0,1,1]
	s_add_u32 s24, s14, 0x48000
	s_min_u32 s24, s24, 0x2e8000
	v_lshl_add_u64 v[210:211], v[4:5], 0, s[24:25]
	v_add_co_u32_e32 v212, vcc, s16, v210
	global_load_dword v194, v[210:211], off
	s_nop 0
	v_addc_co_u32_e32 v213, vcc, 0, v211, vcc
	v_add_co_u32_e32 v214, vcc, s5, v210
	s_nop 1
	v_addc_co_u32_e32 v215, vcc, 0, v211, vcc
	v_add_co_u32_e32 v216, vcc, s18, v210
	s_nop 1
	v_addc_co_u32_e32 v217, vcc, 0, v211, vcc
	global_load_dword v196, v[212:213], off
	global_load_dword v198, v[214:215], off
	global_load_dword v200, v[216:217], off
	v_mov_b32_e32 v3, s17
	ds_read_b128 v[42:45], v3
	ds_read_b128 v[46:49], v3 offset:16
	ds_read_b128 v[50:53], v3 offset:32
	ds_read_b128 v[54:57], v3 offset:48
	ds_read_b128 v[58:61], v3 offset:64
	ds_read_b128 v[62:65], v3 offset:80
	ds_read_b128 v[66:69], v3 offset:96
	ds_read_b128 v[70:73], v3 offset:112
	ds_read_b128 v[74:77], v3 offset:128
	ds_read_b128 v[78:81], v3 offset:144
	ds_read_b128 v[82:85], v3 offset:160
	ds_read_b128 v[86:89], v3 offset:176
	ds_read_b128 v[90:93], v3 offset:192
	ds_read_b128 v[94:97], v3 offset:208
	ds_read_b128 v[98:101], v3 offset:224
	ds_read_b128 v[102:105], v3 offset:240
	ds_read_b128 v[106:109], v3 offset:256
	ds_read_b128 v[110:113], v3 offset:272
	ds_read_b128 v[114:117], v3 offset:288
	ds_read_b128 v[118:121], v3 offset:304
	ds_read_b128 v[122:125], v3 offset:320
	ds_read_b128 v[126:129], v3 offset:336
	ds_read_b128 v[130:133], v3 offset:352
	ds_read_b128 v[134:137], v3 offset:368
	ds_read_b128 v[138:141], v3 offset:384
	ds_read_b128 v[142:145], v3 offset:400
	ds_read_b128 v[146:149], v3 offset:416
	ds_read_b128 v[150:153], v3 offset:432
	ds_read_b128 v[154:157], v3 offset:448
	ds_read_b128 v[158:161], v3 offset:464
	ds_read_b128 v[162:165], v3 offset:480
	ds_read_b128 v[166:169], v3 offset:496
	s_addk_i32 s17, 0x200
	s_add_u32 s14, s14, 0x18000
	s_addc_u32 s15, s15, 0
	s_cmp_eq_u32 s14, 0x300000
	s_waitcnt vmcnt(15) lgkmcnt(14)
	v_pk_fma_f32 v[8:9], v[202:203], v[42:43], v[8:9] op_sel_hi:[0,1,1]
	v_pk_fma_f32 v[10:11], v[202:203], v[44:45], v[10:11] op_sel_hi:[0,1,1]
	v_pk_fma_f32 v[12:13], v[202:203], v[46:47], v[12:13] op_sel_hi:[0,1,1]
	v_pk_fma_f32 v[14:15], v[202:203], v[48:49], v[14:15] op_sel_hi:[0,1,1]
	v_pk_fma_f32 v[16:17], v[202:203], v[50:51], v[16:17] op_sel_hi:[0,1,1]
	v_pk_fma_f32 v[18:19], v[202:203], v[52:53], v[18:19] op_sel_hi:[0,1,1]
	v_pk_fma_f32 v[20:21], v[202:203], v[54:55], v[20:21] op_sel_hi:[0,1,1]
	v_pk_fma_f32 v[22:23], v[202:203], v[56:57], v[22:23] op_sel_hi:[0,1,1]
	v_pk_fma_f32 v[24:25], v[202:203], v[58:59], v[24:25] op_sel_hi:[0,1,1]
	v_pk_fma_f32 v[26:27], v[202:203], v[60:61], v[26:27] op_sel_hi:[0,1,1]
	v_pk_fma_f32 v[28:29], v[202:203], v[62:63], v[28:29] op_sel_hi:[0,1,1]
	v_pk_fma_f32 v[30:31], v[202:203], v[64:65], v[30:31] op_sel_hi:[0,1,1]
	v_pk_fma_f32 v[32:33], v[202:203], v[66:67], v[32:33] op_sel_hi:[0,1,1]
	v_pk_fma_f32 v[34:35], v[202:203], v[68:69], v[34:35] op_sel_hi:[0,1,1]
	v_pk_fma_f32 v[36:37], v[202:203], v[70:71], v[36:37] op_sel_hi:[0,1,1]
	v_pk_fma_f32 v[6:7], v[202:203], v[72:73], v[6:7] op_sel_hi:[0,1,1]
	s_waitcnt vmcnt(14)
	v_pk_fma_f32 v[8:9], v[204:205], v[74:75], v[8:9] op_sel_hi:[0,1,1]
	v_pk_fma_f32 v[10:11], v[204:205], v[76:77], v[10:11] op_sel_hi:[0,1,1]
	v_pk_fma_f32 v[12:13], v[204:205], v[78:79], v[12:13] op_sel_hi:[0,1,1]
	v_pk_fma_f32 v[14:15], v[204:205], v[80:81], v[14:15] op_sel_hi:[0,1,1]
	v_pk_fma_f32 v[16:17], v[204:205], v[82:83], v[16:17] op_sel_hi:[0,1,1]
	v_pk_fma_f32 v[18:19], v[204:205], v[84:85], v[18:19] op_sel_hi:[0,1,1]
	v_pk_fma_f32 v[20:21], v[204:205], v[86:87], v[20:21] op_sel_hi:[0,1,1]
	v_pk_fma_f32 v[22:23], v[204:205], v[88:89], v[22:23] op_sel_hi:[0,1,1]
	v_pk_fma_f32 v[24:25], v[204:205], v[90:91], v[24:25] op_sel_hi:[0,1,1]
	v_pk_fma_f32 v[26:27], v[204:205], v[92:93], v[26:27] op_sel_hi:[0,1,1]
	v_pk_fma_f32 v[28:29], v[204:205], v[94:95], v[28:29] op_sel_hi:[0,1,1]
	v_pk_fma_f32 v[30:31], v[204:205], v[96:97], v[30:31] op_sel_hi:[0,1,1]
	v_pk_fma_f32 v[32:33], v[204:205], v[98:99], v[32:33] op_sel_hi:[0,1,1]
	v_pk_fma_f32 v[34:35], v[204:205], v[100:101], v[34:35] op_sel_hi:[0,1,1]
	v_pk_fma_f32 v[36:37], v[204:205], v[102:103], v[36:37] op_sel_hi:[0,1,1]
	v_pk_fma_f32 v[6:7], v[204:205], v[104:105], v[6:7] op_sel_hi:[0,1,1]
	s_waitcnt vmcnt(13)
	v_pk_fma_f32 v[8:9], v[206:207], v[106:107], v[8:9] op_sel_hi:[0,1,1]
	v_pk_fma_f32 v[10:11], v[206:207], v[108:109], v[10:11] op_sel_hi:[0,1,1]
	v_pk_fma_f32 v[12:13], v[206:207], v[110:111], v[12:13] op_sel_hi:[0,1,1]
	v_pk_fma_f32 v[14:15], v[206:207], v[112:113], v[14:15] op_sel_hi:[0,1,1]
	s_waitcnt lgkmcnt(13)
	v_pk_fma_f32 v[16:17], v[206:207], v[114:115], v[16:17] op_sel_hi:[0,1,1]
	v_pk_fma_f32 v[18:19], v[206:207], v[116:117], v[18:19] op_sel_hi:[0,1,1]
	s_waitcnt lgkmcnt(12)
	v_pk_fma_f32 v[20:21], v[206:207], v[118:119], v[20:21] op_sel_hi:[0,1,1]
	v_pk_fma_f32 v[22:23], v[206:207], v[120:121], v[22:23] op_sel_hi:[0,1,1]
	s_waitcnt lgkmcnt(11)
	v_pk_fma_f32 v[24:25], v[206:207], v[122:123], v[24:25] op_sel_hi:[0,1,1]
	v_pk_fma_f32 v[26:27], v[206:207], v[124:125], v[26:27] op_sel_hi:[0,1,1]
	s_waitcnt lgkmcnt(10)
	v_pk_fma_f32 v[28:29], v[206:207], v[126:127], v[28:29] op_sel_hi:[0,1,1]
	v_pk_fma_f32 v[30:31], v[206:207], v[128:129], v[30:31] op_sel_hi:[0,1,1]
	s_waitcnt lgkmcnt(9)
	v_pk_fma_f32 v[32:33], v[206:207], v[130:131], v[32:33] op_sel_hi:[0,1,1]
	v_pk_fma_f32 v[34:35], v[206:207], v[132:133], v[34:35] op_sel_hi:[0,1,1]
	s_waitcnt lgkmcnt(8)
	v_pk_fma_f32 v[36:37], v[206:207], v[134:135], v[36:37] op_sel_hi:[0,1,1]
	v_pk_fma_f32 v[6:7], v[206:207], v[136:137], v[6:7] op_sel_hi:[0,1,1]
	s_waitcnt vmcnt(12) lgkmcnt(7)
	v_pk_fma_f32 v[8:9], v[208:209], v[138:139], v[8:9] op_sel_hi:[0,1,1]
	v_pk_fma_f32 v[10:11], v[208:209], v[140:141], v[10:11] op_sel_hi:[0,1,1]
	s_waitcnt lgkmcnt(6)
	v_pk_fma_f32 v[12:13], v[208:209], v[142:143], v[12:13] op_sel_hi:[0,1,1]
	v_pk_fma_f32 v[14:15], v[208:209], v[144:145], v[14:15] op_sel_hi:[0,1,1]
	s_waitcnt lgkmcnt(5)
	v_pk_fma_f32 v[16:17], v[208:209], v[146:147], v[16:17] op_sel_hi:[0,1,1]
	v_pk_fma_f32 v[18:19], v[208:209], v[148:149], v[18:19] op_sel_hi:[0,1,1]
	s_waitcnt lgkmcnt(4)
	v_pk_fma_f32 v[20:21], v[208:209], v[150:151], v[20:21] op_sel_hi:[0,1,1]
	v_pk_fma_f32 v[22:23], v[208:209], v[152:153], v[22:23] op_sel_hi:[0,1,1]
	s_waitcnt lgkmcnt(3)
	v_pk_fma_f32 v[24:25], v[208:209], v[154:155], v[24:25] op_sel_hi:[0,1,1]
	v_pk_fma_f32 v[26:27], v[208:209], v[156:157], v[26:27] op_sel_hi:[0,1,1]
	s_waitcnt lgkmcnt(2)
	v_pk_fma_f32 v[28:29], v[208:209], v[158:159], v[28:29] op_sel_hi:[0,1,1]
	v_pk_fma_f32 v[30:31], v[208:209], v[160:161], v[30:31] op_sel_hi:[0,1,1]
	s_waitcnt lgkmcnt(1)
	v_pk_fma_f32 v[32:33], v[208:209], v[162:163], v[32:33] op_sel_hi:[0,1,1]
	v_pk_fma_f32 v[34:35], v[208:209], v[164:165], v[34:35] op_sel_hi:[0,1,1]
	s_waitcnt lgkmcnt(0)
	v_pk_fma_f32 v[36:37], v[208:209], v[166:167], v[36:37] op_sel_hi:[0,1,1]
	v_pk_fma_f32 v[6:7], v[208:209], v[168:169], v[6:7] op_sel_hi:[0,1,1]
	s_cbranch_scc0 .LBB0_12
	s_waitcnt vmcnt(0)
	v_readlane_b32 s5, v252, 46
	s_lshl_b32 s5, s5, 13
	s_add_i32 s5, s5, 0
	s_and_b64 s[14:15], s[0:1], exec
	v_readlane_b32 s16, v252, 13
	v_add_u32_e32 v3, s5, v2
	s_cselect_b32 s5, 0x1800, 0
	v_readlane_b32 s24, v252, 21
	v_readlane_b32 s25, v252, 22
	s_add_i32 s4, s4, s5
	v_mov_b32_e32 v4, s24
	v_mov_b32_e32 v5, s25
	s_barrier
	ds_write2st64_b32 v3, v8, v9 offset1:1
	ds_write2st64_b32 v3, v10, v11 offset0:2 offset1:3
	ds_write2st64_b32 v3, v12, v13 offset0:4 offset1:5
	ds_write2st64_b32 v3, v14, v15 offset0:6 offset1:7
	ds_write2st64_b32 v3, v16, v17 offset0:8 offset1:9
	ds_write2st64_b32 v3, v18, v19 offset0:10 offset1:11
	ds_write2st64_b32 v3, v20, v21 offset0:12 offset1:13
	ds_write2st64_b32 v3, v22, v23 offset0:14 offset1:15
	ds_write2st64_b32 v3, v24, v25 offset0:16 offset1:17
	ds_write2st64_b32 v3, v26, v27 offset0:18 offset1:19
	ds_write2st64_b32 v3, v28, v29 offset0:20 offset1:21
	ds_write2st64_b32 v3, v30, v31 offset0:22 offset1:23
	ds_write2st64_b32 v3, v32, v33 offset0:24 offset1:25
	ds_write2st64_b32 v3, v34, v35 offset0:26 offset1:27
	ds_write2st64_b32 v3, v36, v37 offset0:28 offset1:29
	ds_write2st64_b32 v3, v6, v7 offset0:30 offset1:31
	v_or_b32_e32 v6, s4, v174
	v_mov_b32_e32 v7, 0
	v_lshl_add_u64 v[4:5], v[6:7], 2, v[4:5]
	s_waitcnt lgkmcnt(0)
	s_barrier
	global_load_dword v14, v[4:5], off
	v_add_u32_e32 v15, 0, v2
	v_and_b32_e32 v2, 0x1c0, v0
	v_lshl_add_u32 v6, v2, 2, v15
	ds_read2st64_b32 v[2:3], v6 offset1:32
	ds_read2st64_b32 v[8:9], v6 offset0:64 offset1:96
	ds_read2st64_b32 v[10:11], v6 offset0:128 offset1:160
	ds_read2st64_b32 v[12:13], v6 offset0:192 offset1:224
	s_and_b64 s[0:1], s[0:1], exec
	s_waitcnt lgkmcnt(3)
	v_add_f32_e32 v2, 0, v2
	v_add_f32_e32 v17, v2, v3
	s_waitcnt lgkmcnt(2)
	v_add_f32_e32 v8, v17, v8
	v_add_f32_e32 v8, v8, v9
	s_waitcnt lgkmcnt(1)
	v_add_f32_e32 v8, v8, v10
	s_cselect_b32 s5, 32, 0
	s_add_u32 s0, s92, s2
	v_readlane_b32 s1, v252, 49
	v_add_f32_e32 v8, v8, v11
	v_lshrrev_b32_e32 v16, 6, v0
	v_lshlrev_b32_e32 v6, 2, v174
	s_addc_u32 s1, s1, s3
	s_waitcnt lgkmcnt(0)
	v_add_f32_e32 v8, v8, v12
	s_movk_i32 s4, 0x6000
	v_or_b32_e32 v16, s5, v16
	v_lshl_add_u64 v[6:7], s[0:1], 0, v[6:7]
	v_add_f32_e32 v8, v8, v13
	v_mad_u64_u32 v[2:3], s[0:1], v16, s4, v[6:7]
	v_lshrrev_b32_e32 v16, 6, v40
	v_or_b32_e32 v16, s5, v16
	s_mov_b64 s[2:3], 0
	v_readlane_b32 s17, v252, 14
	v_readlane_b32 s18, v252, 15
	v_readlane_b32 s19, v252, 16
	v_readlane_b32 s20, v252, 17
	v_readlane_b32 s21, v252, 18
	v_readlane_b32 s22, v252, 19
	v_readlane_b32 s23, v252, 20
	v_readlane_b32 s26, v252, 23
	v_readlane_b32 s27, v252, 24
	v_readlane_b32 s28, v252, 25
	v_readlane_b32 s29, v252, 26
	v_readlane_b32 s30, v252, 27
	v_readlane_b32 s31, v252, 28
	s_waitcnt vmcnt(0)
	v_add_f32_e32 v8, v8, v14
	global_store_dword v[2:3], v8, off
	global_load_dword v14, v[4:5], off
	v_and_b32_e32 v2, 0x3c0, v40
	v_lshl_add_u32 v12, v2, 2, v15
	ds_read2st64_b32 v[2:3], v12 offset1:32
	ds_read2st64_b32 v[8:9], v12 offset0:64 offset1:96
	ds_read2st64_b32 v[10:11], v12 offset0:128 offset1:160
	ds_read2st64_b32 v[12:13], v12 offset0:192 offset1:224
	s_waitcnt lgkmcnt(3)
	v_add_f32_e32 v2, 0, v2
	v_add_f32_e32 v17, v2, v3
	s_waitcnt lgkmcnt(2)
	v_add_f32_e32 v8, v17, v8
	v_add_f32_e32 v8, v8, v9
	s_waitcnt lgkmcnt(1)
	v_add_f32_e32 v8, v8, v10
	v_add_f32_e32 v8, v8, v11
	s_waitcnt lgkmcnt(0)
	v_add_f32_e32 v8, v8, v12
	v_add_f32_e32 v8, v8, v13
	v_mad_u64_u32 v[2:3], s[0:1], v16, s4, v[6:7]
	s_movk_i32 s0, 0x5c0
	s_waitcnt vmcnt(0)
	v_add_f32_e32 v8, v8, v14
	global_store_dword v[2:3], v8, off
	global_load_dword v14, v[4:5], off
	v_mov_b32_e32 v3, 0x400
	v_bitop3_b32 v3, v0, s0, v3 bitop3:0xc8
	v_or_b32_e32 v2, 0x400, v0
	v_lshl_add_u32 v12, v3, 2, v15
	v_lshrrev_b32_e32 v16, 6, v2
	ds_read2st64_b32 v[2:3], v12 offset1:32
	ds_read2st64_b32 v[8:9], v12 offset0:64 offset1:96
	ds_read2st64_b32 v[10:11], v12 offset0:128 offset1:160
	ds_read2st64_b32 v[12:13], v12 offset0:192 offset1:224
	v_or_b32_e32 v16, s5, v16
	s_waitcnt lgkmcnt(3)
	v_add_f32_e32 v2, 0, v2
	v_add_f32_e32 v17, v2, v3
	s_waitcnt lgkmcnt(2)
	v_add_f32_e32 v8, v17, v8
	v_add_f32_e32 v8, v8, v9
	s_waitcnt lgkmcnt(1)
	v_add_f32_e32 v8, v8, v10
	v_add_f32_e32 v8, v8, v11
	s_waitcnt lgkmcnt(0)
	v_add_f32_e32 v8, v8, v12
	v_add_f32_e32 v8, v8, v13
	v_mad_u64_u32 v[2:3], s[0:1], v16, s4, v[6:7]
	s_waitcnt vmcnt(0)
	v_add_f32_e32 v8, v8, v14
	global_store_dword v[2:3], v8, off
	global_load_dword v12, v[4:5], off
	v_and_b32_e32 v2, 0x7c0, v1
	v_lshl_add_u32 v10, v2, 2, v15
	ds_read2st64_b32 v[2:3], v10 offset1:32
	ds_read2st64_b32 v[4:5], v10 offset0:64 offset1:96
	ds_read2st64_b32 v[8:9], v10 offset0:128 offset1:160
	ds_read2st64_b32 v[10:11], v10 offset0:192 offset1:224
	v_lshrrev_b32_e32 v1, 6, v1
	s_waitcnt lgkmcnt(3)
	v_add_f32_e32 v2, 0, v2
	v_or_b32_e32 v1, s5, v1
	v_add_f32_e32 v13, v2, v3
	v_mad_u64_u32 v[2:3], s[0:1], v1, s4, v[6:7]
	s_waitcnt lgkmcnt(2)
	v_add_f32_e32 v1, v13, v4
	v_add_f32_e32 v1, v1, v5
	s_waitcnt lgkmcnt(1)
	v_add_f32_e32 v1, v1, v8
	v_add_f32_e32 v1, v1, v9
	s_waitcnt lgkmcnt(0)
	v_add_f32_e32 v1, v1, v10
	v_add_f32_e32 v1, v1, v11
	s_waitcnt vmcnt(0)
	v_add_f32_e32 v1, v1, v12
	global_store_dword v[2:3], v1, off
	s_waitcnt vmcnt(0)
	s_barrier
	s_and_saveexec_b64 s[0:1], s[74:75]
	s_mov_b32 s59, s34
	s_mov_b32 s58, s35
	s_cbranch_execz .LBB0_17
	s_mov_b64 s[2:3], exec
	buffer_wbl2 sc1
	s_waitcnt vmcnt(0)
	s_waitcnt vmcnt(0)
	v_mbcnt_lo_u32_b32 v1, s2, 0
	v_mbcnt_hi_u32_b32 v1, s3, v1
	v_cmp_eq_u32_e32 vcc, 0, v1
	s_and_saveexec_b64 s[4:5], vcc
	s_cbranch_execz .LBB0_16
	s_bcnt1_i32_b64 s2, s[2:3]
	v_mov_b32_e32 v1, 0
	v_mov_b32_e32 v2, s2
	global_atomic_add v1, v2, s[10:11]
